# v17_tailmfma
# speedup vs baseline: 1.0385x; 1.0023x over previous
.LBB2_57:
	ds_read2_b32 v[8:9], v21 offset1:4
	ds_read2_b32 v[30:31], v20 offset1:80
	ds_read2_b32 v[32:33], v22 offset1:4
	s_add_i32 s18, s18, 1
	v_add_u32_e32 v4, 0x8000, v4
	s_add_i32 s2, s2, 64
	s_and_b64 vcc, exec, s[12:13]
	ds_read2_b32 v[136:137], v21 offset0:8 offset1:12
	ds_read2_b32 v[138:139], v20 offset0:160 offset1:240
	ds_read2_b32 v[140:141], v22 offset0:8 offset1:12
	s_waitcnt lgkmcnt(3)
	v_mfma_f32_16x16x4_f32 a[0:3], v8, v30, a[0:3]
	v_mfma_f32_16x16x4_f32 a[4:7], v32, v30, a[4:7]
	v_mfma_f32_16x16x4_f32 a[0:3], v9, v31, a[0:3]
	v_mfma_f32_16x16x4_f32 a[4:7], v33, v31, a[4:7]
	ds_read2_b32 v[8:9], v21 offset0:16 offset1:20
	ds_read2_b32 v[30:31], v24 offset0:64 offset1:144
	ds_read2_b32 v[32:33], v22 offset0:16 offset1:20
	s_waitcnt lgkmcnt(3)
	v_mfma_f32_16x16x4_f32 a[0:3], v136, v138, a[0:3]
	v_mfma_f32_16x16x4_f32 a[4:7], v140, v138, a[4:7]
	v_mfma_f32_16x16x4_f32 a[0:3], v137, v139, a[0:3]
	v_mfma_f32_16x16x4_f32 a[4:7], v141, v139, a[4:7]
	ds_read2_b32 v[136:137], v21 offset0:24 offset1:28
	ds_read2_b32 v[138:139], v25 offset0:96 offset1:176
	ds_read2_b32 v[140:141], v22 offset0:24 offset1:28
	s_waitcnt lgkmcnt(3)
	v_mfma_f32_16x16x4_f32 a[0:3], v8, v30, a[0:3]
	v_mfma_f32_16x16x4_f32 a[4:7], v32, v30, a[4:7]
	v_mfma_f32_16x16x4_f32 a[0:3], v9, v31, a[0:3]
	v_mfma_f32_16x16x4_f32 a[4:7], v33, v31, a[4:7]
	ds_read2_b32 v[8:9], v21 offset0:32 offset1:36
	ds_read2_b32 v[30:31], v26 offset0:128 offset1:208
	ds_read2_b32 v[32:33], v22 offset0:32 offset1:36
	s_waitcnt lgkmcnt(3)
	v_mfma_f32_16x16x4_f32 a[0:3], v136, v138, a[0:3]
	v_mfma_f32_16x16x4_f32 a[4:7], v140, v138, a[4:7]
	v_mfma_f32_16x16x4_f32 a[0:3], v137, v139, a[0:3]
	v_mfma_f32_16x16x4_f32 a[4:7], v141, v139, a[4:7]
	ds_read2_b32 v[136:137], v21 offset0:40 offset1:44
	ds_read2_b32 v[138:139], v27 offset0:32 offset1:112
	ds_read2_b32 v[140:141], v22 offset0:40 offset1:44
	s_waitcnt lgkmcnt(3)
	v_mfma_f32_16x16x4_f32 a[0:3], v8, v30, a[0:3]
	v_mfma_f32_16x16x4_f32 a[4:7], v32, v30, a[4:7]
	v_mfma_f32_16x16x4_f32 a[0:3], v9, v31, a[0:3]
	v_mfma_f32_16x16x4_f32 a[4:7], v33, v31, a[4:7]
	ds_read2_b32 v[8:9], v21 offset0:48 offset1:52
	ds_read2_b32 v[30:31], v28 offset0:64 offset1:144
	ds_read2_b32 v[32:33], v22 offset0:48 offset1:52
	s_waitcnt lgkmcnt(3)
	v_mfma_f32_16x16x4_f32 a[0:3], v136, v138, a[0:3]
	v_mfma_f32_16x16x4_f32 a[4:7], v140, v138, a[4:7]
	v_mfma_f32_16x16x4_f32 a[0:3], v137, v139, a[0:3]
	v_mfma_f32_16x16x4_f32 a[4:7], v141, v139, a[4:7]
	ds_read2_b32 v[136:137], v21 offset0:56 offset1:60
	ds_read2_b32 v[138:139], v29 offset0:96 offset1:176
	ds_read2_b32 v[140:141], v22 offset0:56 offset1:60
	s_waitcnt lgkmcnt(3)
	v_mfma_f32_16x16x4_f32 a[0:3], v8, v30, a[0:3]
	v_mfma_f32_16x16x4_f32 a[4:7], v32, v30, a[4:7]
	v_mfma_f32_16x16x4_f32 a[0:3], v9, v31, a[0:3]
	v_mfma_f32_16x16x4_f32 a[4:7], v33, v31, a[4:7]
	s_waitcnt lgkmcnt(0)
	v_mfma_f32_16x16x4_f32 a[0:3], v136, v138, a[0:3]
	v_mfma_f32_16x16x4_f32 a[4:7], v140, v138, a[4:7]
	v_mfma_f32_16x16x4_f32 a[0:3], v137, v139, a[0:3]
	v_mfma_f32_16x16x4_f32 a[4:7], v141, v139, a[4:7]
	s_cbranch_vccnz .LBB2_68

	.amdhsa_kernel _Z6k_tailPKfPfS1_S0_S1_PDF16_S1_
		.amdhsa_group_segment_fixed_size 79872
		.amdhsa_private_segment_fixed_size 0
		.amdhsa_kernarg_size 56
		.amdhsa_user_sgpr_count 2
		.amdhsa_user_sgpr_dispatch_ptr 0
		.amdhsa_user_sgpr_queue_ptr 0
		.amdhsa_user_sgpr_kernarg_segment_ptr 1
		.amdhsa_user_sgpr_dispatch_id 0
		.amdhsa_user_sgpr_kernarg_preload_length 0
		.amdhsa_user_sgpr_kernarg_preload_offset 0
		.amdhsa_user_sgpr_private_segment_size 0
		.amdhsa_uses_dynamic_stack 0
		.amdhsa_enable_private_segment 0
		.amdhsa_system_sgpr_workgroup_id_x 1
		.amdhsa_system_sgpr_workgroup_id_y 0
		.amdhsa_system_sgpr_workgroup_id_z 0
		.amdhsa_system_sgpr_workgroup_info 0
		.amdhsa_system_vgpr_workitem_id 0
		.amdhsa_next_free_vgpr 177
		.amdhsa_next_free_sgpr 96
		.amdhsa_accum_offset 144
		.amdhsa_reserve_vcc 1
		.amdhsa_float_round_mode_32 0
		.amdhsa_float_round_mode_16_64 0
		.amdhsa_float_denorm_mode_32 3
		.amdhsa_float_denorm_mode_16_64 3
		.amdhsa_dx10_clamp 1
		.amdhsa_ieee_mode 1
		.amdhsa_fp16_overflow 0
		.amdhsa_tg_split 0
		.amdhsa_exception_fp_ieee_invalid_op 0
		.amdhsa_exception_fp_denorm_src 0
		.amdhsa_exception_fp_ieee_div_zero 0
		.amdhsa_exception_fp_ieee_overflow 0
		.amdhsa_exception_fp_ieee_underflow 0
		.amdhsa_exception_fp_ieee_inexact 0
		.amdhsa_exception_int_div_zero 0
	.end_amdhsa_kernel

amdhsa.kernels:
  - .agpr_count:     16
    .args:
      - .actual_access:  read_only
        .address_space:  global
        .offset:         0
        .size:           8
        .value_kind:     global_buffer
      - .actual_access:  read_only
        .address_space:  global
        .offset:         8
        .size:           8
        .value_kind:     global_buffer
      - .actual_access:  read_only
        .address_space:  global
        .offset:         16
        .size:           8
        .value_kind:     global_buffer
      - .actual_access:  write_only
        .address_space:  global
        .offset:         24
        .size:           8
        .value_kind:     global_buffer
      - .actual_access:  write_only
        .address_space:  global
        .offset:         32
        .size:           8
        .value_kind:     global_buffer
      - .actual_access:  write_only
        .address_space:  global
        .offset:         40
        .size:           8
        .value_kind:     global_buffer
    .group_segment_fixed_size: 18944
    .kernarg_segment_align: 8
    .kernarg_segment_size: 48
    .language:       OpenCL C
    .language_version:
      - 2
      - 0
    .max_flat_workgroup_size: 256
    .name:           _Z9k_gemm_byPKfS0_S0_PfS1_Pd
    .private_segment_fixed_size: 0
    .sgpr_count:     22
    .sgpr_spill_count: 0
    .symbol:         _Z9k_gemm_byPKfS0_S0_PfS1_Pd.kd
    .uniform_work_group_size: 1
    .uses_dynamic_stack: false
    .vgpr_count:     168
    .vgpr_spill_count: 0
    .wavefront_size: 64
  - .agpr_count:     48
    .args:
      - .address_space:  global
        .offset:         0
        .size:           8
        .value_kind:     global_buffer
      - .address_space:  global
        .offset:         8
        .size:           8
        .value_kind:     global_buffer
      - .address_space:  global
        .offset:         16
        .size:           8
        .value_kind:     global_buffer
      - .address_space:  global
        .offset:         24
        .size:           8
        .value_kind:     global_buffer
      - .actual_access:  write_only
        .address_space:  global
        .offset:         32
        .size:           8
        .value_kind:     global_buffer
      - .offset:         40
        .size:           4
        .value_kind:     by_value
      - .actual_access:  read_only
        .address_space:  global
        .offset:         48
        .size:           8
        .value_kind:     global_buffer
      - .actual_access:  read_only
        .address_space:  global
        .offset:         56
        .size:           8
        .value_kind:     global_buffer
      - .actual_access:  read_only
        .address_space:  global
        .offset:         64
        .size:           8
        .value_kind:     global_buffer
      - .address_space:  global
        .offset:         72
        .size:           8
        .value_kind:     global_buffer
      - .offset:         80
        .size:           4
        .value_kind:     by_value
      - .actual_access:  write_only
        .address_space:  global
        .offset:         88
        .size:           8
        .value_kind:     global_buffer
      - .actual_access:  write_only
        .address_space:  global
        .offset:         96
        .size:           8
        .value_kind:     global_buffer
      - .actual_access:  write_only
        .address_space:  global
        .offset:         104
        .size:           8
        .value_kind:     global_buffer
    .group_segment_fixed_size: 139520
    .kernarg_segment_align: 8
    .kernarg_segment_size: 112
    .language:       OpenCL C
    .language_version:
      - 2
      - 0
    .max_flat_workgroup_size: 256
    .name:           _Z7k_chol2PfS_S_S_PdiPKfS2_S2_S_iS_PDF16_S_
    .private_segment_fixed_size: 0
    .sgpr_count:     106
    .sgpr_spill_count: 0
    .symbol:         _Z7k_chol2PfS_S_S_PdiPKfS2_S2_S_iS_PDF16_S_.kd
    .uniform_work_group_size: 1
    .uses_dynamic_stack: false
    .vgpr_count:     252
    .vgpr_spill_count: 0
    .wavefront_size: 64
  - .agpr_count:     16
    .args:
      - .actual_access:  read_only
        .address_space:  global
        .offset:         0
        .size:           8
        .value_kind:     global_buffer
      - .address_space:  global
        .offset:         8
        .size:           8
        .value_kind:     global_buffer
      - .address_space:  global
        .offset:         16
        .size:           8
        .value_kind:     global_buffer
      - .actual_access:  read_only
        .address_space:  global
        .offset:         24
        .size:           8
        .value_kind:     global_buffer
      - .actual_access:  write_only
        .address_space:  global
        .offset:         32
        .size:           8
        .value_kind:     global_buffer
      - .actual_access:  write_only
        .address_space:  global
        .offset:         40
        .size:           8
        .value_kind:     global_buffer
      - .actual_access:  write_only
        .address_space:  global
        .offset:         48
        .size:           8
        .value_kind:     global_buffer
    .group_segment_fixed_size: 79872
    .kernarg_segment_align: 8
    .kernarg_segment_size: 56
    .language:       OpenCL C
    .language_version:
      - 2
      - 0
    .max_flat_workgroup_size: 256
    .name:           _Z6k_tailPKfPfS1_S0_S1_PDF16_S1_
    .private_segment_fixed_size: 0
    .sgpr_count:     34
    .sgpr_spill_count: 0
    .symbol:         _Z6k_tailPKfPfS1_S0_S1_PDF16_S1_.kd
    .uniform_work_group_size: 1
    .uses_dynamic_stack: false
    .vgpr_count:     160
    .vgpr_spill_count: 0
    .wavefront_size: 64
  - .agpr_count:     0
    .args:
      - .actual_access:  read_only
        .address_space:  global
        .offset:         0
        .size:           8
        .value_kind:     global_buffer
      - .actual_access:  read_only
        .address_space:  global
        .offset:         8
        .size:           8
        .value_kind:     global_buffer
      - .actual_access:  read_only
        .address_space:  global
        .offset:         16
        .size:           8
        .value_kind:     global_buffer
      - .actual_access:  write_only
        .address_space:  global
        .offset:         24
        .size:           8
        .value_kind:     global_buffer
      - .actual_access:  write_only
        .address_space:  global
        .offset:         32
        .size:           8
        .value_kind:     global_buffer
      - .actual_access:  write_only
        .address_space:  global
        .offset:         40
        .size:           8
        .value_kind:     global_buffer
    .group_segment_fixed_size: 16896
    .kernarg_segment_align: 8
    .kernarg_segment_size: 48
    .language:       OpenCL C
    .language_version:
      - 2
      - 0
    .max_flat_workgroup_size: 256
    .name:           _Z6k_prepPKfS0_S0_PfPDF16_S1_
    .private_segment_fixed_size: 0
    .sgpr_count:     28
    .sgpr_spill_count: 0
    .symbol:         _Z6k_prepPKfS0_S0_PfPDF16_S1_.kd
    .uniform_work_group_size: 1
    .uses_dynamic_stack: false
    .vgpr_count:     150
    .vgpr_spill_count: 0
    .wavefront_size: 64
  - .agpr_count:     0
    .args:
      - .actual_access:  read_only
        .address_space:  global
        .offset:         0
        .size:           8
        .value_kind:     global_buffer
      - .actual_access:  read_only
        .address_space:  global
        .offset:         8
        .size:           8
        .value_kind:     global_buffer
      - .actual_access:  read_only
        .address_space:  global
        .offset:         16
        .size:           8
        .value_kind:     global_buffer
      - .actual_access:  read_only
        .address_space:  global
        .offset:         24
        .size:           8
        .value_kind:     global_buffer
      - .actual_access:  write_only
        .address_space:  global
        .offset:         32
        .size:           8
        .value_kind:     global_buffer
      - .actual_access:  write_only
        .address_space:  global
        .offset:         40
        .size:           8
        .value_kind:     global_buffer
    .group_segment_fixed_size: 111616
    .kernarg_segment_align: 8
    .kernarg_segment_size: 48
    .language:       OpenCL C
    .language_version:
      - 2
      - 0
    .max_flat_workgroup_size: 512
    .name:           _Z6k_mainPKfS0_PKDF16_S0_PfPd
    .private_segment_fixed_size: 0
    .sgpr_count:     25
    .sgpr_spill_count: 0
    .symbol:         _Z6k_mainPKfS0_PKDF16_S0_PfPd.kd
    .uniform_work_group_size: 1
    .uses_dynamic_stack: false
    .vgpr_count:     246
    .vgpr_spill_count: 0
    .wavefront_size: 64
  - .agpr_count:     0
    .args:
      - .actual_access:  read_only
        .address_space:  global
        .offset:         0
        .size:           8
        .value_kind:     global_buffer
      - .actual_access:  write_only
        .address_space:  global
        .offset:         8
        .size:           8
        .value_kind:     global_buffer
    .group_segment_fixed_size: 0
    .kernarg_segment_align: 8
    .kernarg_segment_size: 16
    .language:       OpenCL C
    .language_version:
      - 2
      - 0
    .max_flat_workgroup_size: 1024
    .name:           _Z7k_finalPKdPf
    .private_segment_fixed_size: 0
    .sgpr_count:     28
    .sgpr_spill_count: 0
    .symbol:         _Z7k_finalPKdPf.kd
    .uniform_work_group_size: 1
    .uses_dynamic_stack: false
    .vgpr_count:     60
    .vgpr_spill_count: 0
    .wavefront_size: 64
